# assign/gather token loop: the 8 loop-invariant norm_moe weight vectors loaded once before the loop instead of per token; counted waits re-derived
# baseline (speedup 1.0000x reference)
.LBB0_2466:
	s_or_b64 exec, exec, s[16:17]
	s_andn2_b64 vcc, exec, s[8:9]
	s_waitcnt lgkmcnt(0)
	s_barrier
	s_cbranch_vccnz .LBB0_2138
	s_ashr_i32 s11, s10, 31
	s_lshl_b64 s[16:17], s[10:11], 4
	s_add_u32 s16, s84, s16
	s_addc_u32 s17, s85, s17
	s_lshl_b64 s[18:19], s[10:11], 12
	v_lshl_add_u64 v[112:113], v[48:49], 0, s[18:19]
	s_mov_b32 s11, s25
	s_mov_b32 s15, s24
	global_load_dwordx4 v[186:189], v[40:41], off offset:16
	global_load_dwordx4 v[190:193], v[40:41], off
	global_load_dwordx4 v[210:213], v[40:41], off offset:2048
	global_load_dwordx4 v[214:217], v[40:41], off offset:2064
	global_load_dwordx4 v[218:221], v[42:43], off
	global_load_dwordx4 v[222:225], v[42:43], off offset:16
	global_load_dwordx4 v[226:229], v[44:45], off
	global_load_dwordx4 v[230:233], v[44:45], off offset:16
.LBB0_2468:
	global_load_dwordx4 v[150:153], v5, s[16:17]
	global_load_dwordx4 v[154:157], v138, s[16:17]
	global_load_dwordx4 v[158:161], v139, s[16:17]
	global_load_dwordx4 v[162:165], v140, s[16:17]
	global_load_dwordx4 v[166:169], v141, s[16:17]
	global_load_dwordx4 v[170:173], v142, s[16:17]
	global_load_dwordx4 v[174:177], v143, s[16:17]
	global_load_dwordx4 v[178:181], v144, s[16:17]
	global_load_dwordx4 v[182:185], v[112:113], off offset:-3072
	global_load_dwordx4 v[198:201], v[112:113], off offset:-2048
	global_load_dwordx4 v[202:205], v[112:113], off offset:-1024
	global_load_dwordx4 v[206:209], v[112:113], off
	v_mov_b32_e32 v4, s11
	ds_read2_b32 v[114:115], v4 offset1:1
	ds_read2_b32 v[116:117], v4 offset0:2 offset1:3
	v_mov_b32_e32 v194, 0
	v_mov_b32_e32 v195, 0
	s_add_i32 s15, s15, 8
	s_waitcnt lgkmcnt(1)
	v_ashrrev_i32_e32 v119, 31, v114
	v_mov_b32_e32 v118, v114
	v_ashrrev_i32_e32 v121, 31, v115
	v_mov_b32_e32 v120, v115
	s_waitcnt lgkmcnt(0)
	v_ashrrev_i32_e32 v115, 31, v116
	v_mov_b32_e32 v114, v116
	v_ashrrev_i32_e32 v197, 31, v117
	v_mov_b32_e32 v196, v117
	v_lshlrev_b64 v[116:117], 11, v[120:121]
	v_lshlrev_b64 v[118:119], 11, v[118:119]
	v_lshlrev_b64 v[120:121], 11, v[196:197]
	v_lshlrev_b64 v[196:197], 11, v[114:115]
	v_lshl_add_u64 v[114:115], v[46:47], 0, v[118:119]
	v_lshl_add_u64 v[118:119], v[46:47], 0, v[196:197]
	v_lshl_add_u64 v[116:117], v[46:47], 0, v[116:117]
	v_lshl_add_u64 v[120:121], v[46:47], 0, v[120:121]
	s_addk_i32 s11, 0x80
	s_add_u32 s16, s16, 0x80
	s_addc_u32 s17, s17, 0
	s_cmp_gt_u32 s15, 55
	s_waitcnt vmcnt(11)
	v_mov_b32_e32 v196, v150
	s_waitcnt vmcnt(10)
	v_mov_b32_e32 v197, v154
	v_mov_b32_e32 v154, v151
	v_mov_b32_e32 v150, v152
	v_mov_b32_e32 v151, v156
	v_mov_b32_e32 v156, v153
	s_waitcnt vmcnt(9)
	v_mov_b32_e32 v152, v159
	v_mov_b32_e32 v153, v160
	v_mov_b32_e32 v159, v161
	v_pk_add_f32 v[154:155], v[196:197], v[154:155]
	v_pk_add_f32 v[150:151], v[150:151], v[156:157]
	v_pk_add_f32 v[152:153], v[152:153], v[158:159]
	v_pk_add_f32 v[150:151], v[154:155], v[150:151]
	v_pk_add_f32 v[152:153], v[152:153], v[152:153] op_sel:[0,1] op_sel_hi:[1,0]
	v_add_f32_e32 v4, 0, v150
	s_waitcnt vmcnt(8)
	v_add_f32_e32 v160, v162, v163
	v_add_f32_e32 v162, v164, v165
	s_waitcnt vmcnt(7)
	v_mov_b32_e32 v165, v166
	v_mov_b32_e32 v161, v168
	v_mov_b32_e32 v163, v169
	v_mov_b32_e32 v153, v167
	v_add_f32_e32 v164, v4, v151
	s_waitcnt vmcnt(6)
	v_mov_b32_e32 v168, v171
	v_mov_b32_e32 v169, v172
	v_mov_b32_e32 v171, v173
	v_pk_add_f32 v[156:157], v[160:161], v[162:163]
	v_pk_add_f32 v[150:151], v[164:165], v[152:153]
	v_pk_add_f32 v[158:159], v[168:169], v[170:171]
	v_pk_add_f32 v[150:151], v[150:151], v[156:157]
	v_pk_add_f32 v[154:155], v[158:159], v[158:159] op_sel:[0,1] op_sel_hi:[1,0]
	v_pk_add_f32 v[150:151], v[150:151], v[150:151] op_sel:[0,1] op_sel_hi:[1,0]
	s_waitcnt vmcnt(5)
	v_add_f32_e32 v172, v174, v175
	v_add_f32_e32 v174, v176, v177
	s_waitcnt vmcnt(4)
	v_mov_b32_e32 v173, v180
	v_mov_b32_e32 v175, v181
	v_mov_b32_e32 v155, v179
	v_mov_b32_e32 v151, v178
	v_pk_add_f32 v[160:161], v[172:173], v[174:175]
	v_pk_add_f32 v[150:151], v[150:151], v[154:155]
	s_waitcnt vmcnt(3)
	v_lshlrev_b32_e32 v176, 16, v182
	v_pk_add_f32 v[150:151], v[150:151], v[160:161]
	v_and_b32_e32 v177, 0xffff0000, v182
	v_add_f32_e32 v4, v150, v151
	v_fmamk_f32 v4, v4, 0x3a000000, v145
	v_rsq_f32_e32 v4, v4
	v_lshlrev_b32_e32 v180, 16, v183
	v_and_b32_e32 v181, 0xffff0000, v183
	v_lshlrev_b32_e32 v182, 16, v184
	v_and_b32_e32 v183, 0xffff0000, v184
	v_mul_f32_e32 v4, 0x41000000, v4
	v_pk_mul_f32 v[150:151], v[4:5], v[176:177] op_sel_hi:[0,1]
	v_pk_mul_f32 v[152:153], v[4:5], v[180:181] op_sel_hi:[0,1]
	v_pk_mul_f32 v[154:155], v[4:5], v[182:183] op_sel_hi:[0,1]
	s_waitcnt vmcnt(3)
	v_pk_mul_f32 v[152:153], v[192:193], v[152:153]
	v_pk_mul_f32 v[150:151], v[190:191], v[150:151]
	v_pk_mul_f32 v[154:155], v[186:187], v[154:155]
	v_med3_f32 v147, v150, s27, v146
	v_med3_f32 v150, v151, s27, v146
	v_med3_f32 v151, v152, s27, v146
	v_med3_f32 v152, v153, s27, v146
	v_med3_f32 v153, v154, s27, v146
	v_med3_f32 v154, v155, s27, v146
	v_lshlrev_b32_e32 v184, 16, v185
	v_and_b32_e32 v185, 0xffff0000, v185
	v_cvt_pk_fp8_f32 v194, v147, v150
	v_cvt_pk_fp8_f32 v195, v153, v154
	v_pk_mul_f32 v[156:157], v[4:5], v[184:185] op_sel_hi:[0,1]
	v_pk_mul_f32 v[156:157], v[188:189], v[156:157]
	v_cvt_pk_fp8_f32 v194, v151, v152 op_sel:[0,0,1]
	v_med3_f32 v155, v156, s27, v146
	v_med3_f32 v156, v157, s27, v146
	v_cvt_pk_fp8_f32 v195, v155, v156 op_sel:[0,0,1]
	global_store_dwordx2 v[114:115], v[194:195], off
	global_store_dwordx2 v[116:117], v[194:195], off
	global_store_dwordx2 v[118:119], v[194:195], off
	global_store_dwordx2 v[120:121], v[194:195], off
	v_mov_b32_e32 v162, 0
	v_mov_b32_e32 v163, 0
	s_waitcnt vmcnt(6)
	v_lshlrev_b32_e32 v164, 16, v198
	v_and_b32_e32 v165, 0xffff0000, v198
	v_lshlrev_b32_e32 v150, 16, v199
	v_and_b32_e32 v151, 0xffff0000, v199
	v_lshlrev_b32_e32 v166, 16, v200
	v_and_b32_e32 v167, 0xffff0000, v200
	v_pk_mul_f32 v[164:165], v[4:5], v[164:165] op_sel_hi:[0,1]
	v_pk_mul_f32 v[150:151], v[4:5], v[150:151] op_sel_hi:[0,1]
	v_pk_mul_f32 v[166:167], v[4:5], v[166:167] op_sel_hi:[0,1]
	s_waitcnt vmcnt(6)
	v_pk_mul_f32 v[150:151], v[212:213], v[150:151]
	v_pk_mul_f32 v[154:155], v[210:211], v[164:165]
	s_waitcnt vmcnt(6)
	v_pk_mul_f32 v[156:157], v[214:215], v[166:167]
	v_med3_f32 v147, v154, s27, v146
	v_med3_f32 v154, v155, s27, v146
	v_med3_f32 v155, v156, s27, v146
	v_med3_f32 v156, v157, s27, v146
	v_lshlrev_b32_e32 v152, 16, v201
	v_and_b32_e32 v153, 0xffff0000, v201
	v_cvt_pk_fp8_f32 v162, v147, v154
	v_cvt_pk_fp8_f32 v163, v155, v156
	v_pk_mul_f32 v[152:153], v[4:5], v[152:153] op_sel_hi:[0,1]
	v_pk_mul_f32 v[152:153], v[216:217], v[152:153]
	v_med3_f32 v150, v150, s27, v146
	v_med3_f32 v151, v151, s27, v146
	v_med3_f32 v152, v152, s27, v146
	v_med3_f32 v153, v153, s27, v146
	v_cvt_pk_fp8_f32 v162, v150, v151 op_sel:[0,0,1]
	v_cvt_pk_fp8_f32 v163, v152, v153 op_sel:[0,0,1]
	global_store_dwordx2 v[114:115], v[162:163], off offset:512
	global_store_dwordx2 v[116:117], v[162:163], off offset:512
	global_store_dwordx2 v[118:119], v[162:163], off offset:512
	global_store_dwordx2 v[120:121], v[162:163], off offset:512
	v_mov_b32_e32 v162, 0
	v_mov_b32_e32 v163, 0
	s_waitcnt vmcnt(9)
	v_lshlrev_b32_e32 v164, 16, v202
	v_and_b32_e32 v165, 0xffff0000, v202
	v_lshlrev_b32_e32 v150, 16, v203
	v_and_b32_e32 v151, 0xffff0000, v203
	v_lshlrev_b32_e32 v166, 16, v204
	v_and_b32_e32 v167, 0xffff0000, v204
	v_pk_mul_f32 v[164:165], v[4:5], v[164:165] op_sel_hi:[0,1]
	v_pk_mul_f32 v[150:151], v[4:5], v[150:151] op_sel_hi:[0,1]
	v_pk_mul_f32 v[166:167], v[4:5], v[166:167] op_sel_hi:[0,1]
	s_waitcnt vmcnt(9)
	v_pk_mul_f32 v[150:151], v[220:221], v[150:151]
	v_pk_mul_f32 v[154:155], v[218:219], v[164:165]
	s_waitcnt vmcnt(9)
	v_pk_mul_f32 v[156:157], v[222:223], v[166:167]
	v_med3_f32 v147, v154, s27, v146
	v_med3_f32 v154, v155, s27, v146
	v_med3_f32 v155, v156, s27, v146
	v_med3_f32 v156, v157, s27, v146
	v_lshlrev_b32_e32 v152, 16, v205
	v_and_b32_e32 v153, 0xffff0000, v205
	v_cvt_pk_fp8_f32 v162, v147, v154
	v_cvt_pk_fp8_f32 v163, v155, v156
	v_pk_mul_f32 v[152:153], v[4:5], v[152:153] op_sel_hi:[0,1]
	v_pk_mul_f32 v[152:153], v[224:225], v[152:153]
	v_med3_f32 v150, v150, s27, v146
	v_med3_f32 v151, v151, s27, v146
	v_med3_f32 v152, v152, s27, v146
	v_med3_f32 v153, v153, s27, v146
	v_cvt_pk_fp8_f32 v162, v150, v151 op_sel:[0,0,1]
	v_cvt_pk_fp8_f32 v163, v152, v153 op_sel:[0,0,1]
	global_store_dwordx2 v[114:115], v[162:163], off offset:1024
	global_store_dwordx2 v[116:117], v[162:163], off offset:1024
	global_store_dwordx2 v[118:119], v[162:163], off offset:1024
	global_store_dwordx2 v[120:121], v[162:163], off offset:1024
	v_mov_b32_e32 v162, 0
	v_mov_b32_e32 v163, 0
	v_lshl_add_u64 v[112:113], v[112:113], 0, s[12:13]
	s_waitcnt vmcnt(12)
	v_lshlrev_b32_e32 v164, 16, v206
	v_and_b32_e32 v165, 0xffff0000, v206
	v_lshlrev_b32_e32 v150, 16, v207
	v_and_b32_e32 v151, 0xffff0000, v207
	v_lshlrev_b32_e32 v166, 16, v208
	v_and_b32_e32 v167, 0xffff0000, v208
	v_pk_mul_f32 v[164:165], v[4:5], v[164:165] op_sel_hi:[0,1]
	v_pk_mul_f32 v[150:151], v[4:5], v[150:151] op_sel_hi:[0,1]
	v_pk_mul_f32 v[166:167], v[4:5], v[166:167] op_sel_hi:[0,1]
	v_lshlrev_b32_e32 v152, 16, v209
	v_and_b32_e32 v153, 0xffff0000, v209
	s_waitcnt vmcnt(12)
	v_pk_mul_f32 v[150:151], v[228:229], v[150:151]
	v_pk_mul_f32 v[154:155], v[226:227], v[164:165]
	s_waitcnt vmcnt(12)
	v_pk_mul_f32 v[156:157], v[230:231], v[166:167]
	v_pk_mul_f32 v[152:153], v[4:5], v[152:153] op_sel_hi:[0,1]
	v_med3_f32 v4, v154, s27, v146
	v_med3_f32 v147, v155, s27, v146
	v_med3_f32 v154, v156, s27, v146
	v_med3_f32 v155, v157, s27, v146
	v_cvt_pk_fp8_f32 v162, v4, v147
	v_cvt_pk_fp8_f32 v163, v154, v155
	v_pk_mul_f32 v[152:153], v[232:233], v[152:153]
	v_med3_f32 v150, v150, s27, v146
	v_med3_f32 v151, v151, s27, v146
	v_med3_f32 v152, v152, s27, v146
	v_med3_f32 v153, v153, s27, v146
	v_cvt_pk_fp8_f32 v162, v150, v151 op_sel:[0,0,1]
	v_cvt_pk_fp8_f32 v163, v152, v153 op_sel:[0,0,1]
	global_store_dwordx2 v[114:115], v[162:163], off offset:1536
	global_store_dwordx2 v[116:117], v[162:163], off offset:1536
	global_store_dwordx2 v[118:119], v[162:163], off offset:1536
	global_store_dwordx2 v[120:121], v[162:163], off offset:1536
	s_cbranch_scc0 .LBB0_2468
	s_branch .LBB0_2138
